# k_fine: compact run loads (saddr+32bit offset, no branches, plain loads), skip long-run loop when unused, DPP block scans, batched rank/placement LDS chains; plus online-softmax agg2 + stageA edits
# speedup vs baseline: 1.0736x; 1.0266x over previous
.LBB0_2:
	s_or_b64 exec, exec, s[4:5]
	s_movk_i32 s3, 0x80
	v_cmp_gt_u32_e64 s[28:29], s3, v0
	s_and_saveexec_b64 s[4:5], s[28:29]
	v_lshlrev_b32_e32 v1, 2, v0
	v_mov_b32_e32 v2, 0
	ds_write_b32 v1, v2 offset:31744
	s_or_b64 exec, exec, s[4:5]
	v_mbcnt_lo_u32_b32 v1, -1, 0
	v_mbcnt_hi_u32_b32 v3, -1, v1
	v_and_b32_e32 v4, 64, v3
	v_add_u32_e32 v1, -1, v3
	v_cmp_lt_i32_e64 s[4:5], v1, v4
	v_add_u32_e32 v5, -2, v3
	v_lshrrev_b32_e32 v35, 6, v0
	v_cndmask_b32_e64 v1, v1, v3, s[4:5]
	v_lshlrev_b32_e32 v31, 2, v1
	v_and_b32_e32 v1, 63, v0
	v_cmp_eq_u32_e64 s[36:37], 0, v1
	v_cmp_lt_i32_e64 s[4:5], v5, v4
	s_waitcnt lgkmcnt(0)
	v_cndmask_b32_e64 v5, v5, v3, s[4:5]
	v_lshlrev_b32_e32 v32, 2, v5
	v_cmp_gt_u32_e64 s[4:5], 2, v1
	s_waitcnt lgkmcnt(0)
	s_nop 0
	v_add_u32_e32 v5, -4, v3
	v_cmp_lt_i32_e64 s[6:7], v5, v4
	s_nop 1
	v_cndmask_b32_e64 v5, v5, v3, s[6:7]
	v_lshlrev_b32_e32 v33, 2, v5
	v_cmp_gt_u32_e64 s[6:7], 4, v1
	s_waitcnt lgkmcnt(0)
	s_nop 0
	v_add_u32_e32 v5, -8, v3
	v_cmp_lt_i32_e64 s[8:9], v5, v4
	s_nop 1
	v_cndmask_b32_e64 v5, v5, v3, s[8:9]
	v_lshlrev_b32_e32 v34, 2, v5
	v_cmp_gt_u32_e64 s[8:9], 8, v1
	s_waitcnt lgkmcnt(0)
	s_nop 0
	v_add_u32_e32 v5, -16, v3
	v_cmp_lt_i32_e64 s[10:11], v5, v4
	s_nop 1
	v_cndmask_b32_e64 v5, v5, v3, s[10:11]
	v_lshlrev_b32_e32 v36, 2, v5
	v_cmp_gt_u32_e64 s[10:11], 16, v1
	s_waitcnt lgkmcnt(0)
	s_nop 0
	v_subrev_u32_e32 v5, 32, v3
	v_cmp_lt_i32_e64 s[12:13], v5, v4
	s_nop 1
	v_cndmask_b32_e64 v3, v5, v3, s[12:13]
	v_lshlrev_b32_e32 v37, 2, v3
	v_mov_b32_e32 v2, v8
	s_nop 1
	v_add_u32_dpp v2, v2, v2 row_shr:1 row_mask:0xf bank_mask:0xf bound_ctrl:1
	s_nop 1
	v_add_u32_dpp v2, v2, v2 row_shr:2 row_mask:0xf bank_mask:0xf bound_ctrl:1
	s_nop 1
	v_add_u32_dpp v2, v2, v2 row_shr:4 row_mask:0xf bank_mask:0xf bound_ctrl:1
	s_nop 1
	v_add_u32_dpp v2, v2, v2 row_shr:8 row_mask:0xf bank_mask:0xf bound_ctrl:1
	s_nop 1
	v_add_u32_dpp v2, v2, v2 row_bcast:15 row_mask:0xa bank_mask:0xf
	s_nop 1
	v_add_u32_dpp v2, v2, v2 row_bcast:31 row_mask:0xc bank_mask:0xf
	v_mov_b32_e32 v3, 0
	v_cmp_eq_u32_e64 s[12:13], 63, v1
	s_and_saveexec_b64 s[14:15], s[12:13]
	s_cbranch_execz .LBB0_6
	v_lshlrev_b32_e32 v4, 2, v35
	s_waitcnt lgkmcnt(0)
	v_add_u32_e32 v2, v2, v3
	ds_write_b32 v4, v2 offset:32256
.LBB0_6:
	s_or_b64 exec, exec, s[14:15]
	v_mov_b32_e32 v2, 0
	s_waitcnt lgkmcnt(0)
	s_barrier
	ds_read_b96 v[4:6], v2 offset:32256
	v_mov_b32_e32 v3, 0x7e0c
	ds_read_b32 v7, v2 offset:32308
	ds_read_b64 v[10:11], v2 offset:32312
	ds_read2_b32 v[12:13], v3 offset1:1
	v_mov_b32_e32 v9, 0x7e1c
	v_mov_b32_e32 v14, 0x7e2c
	s_waitcnt lgkmcnt(0)
	v_readfirstlane_b32 s33, v4
	v_readfirstlane_b32 s45, v6
	s_waitcnt lgkmcnt(0)
	v_readfirstlane_b32 s46, v7
	v_readfirstlane_b32 s44, v5
	v_mov_b32_e32 v5, 0x7e14
	s_waitcnt lgkmcnt(0)
	ds_read2_b32 v[4:5], v5 offset1:1
	v_readfirstlane_b32 s47, v12
	v_mov_b32_e32 v12, 0x7e24
	v_readfirstlane_b32 s48, v13
	s_waitcnt lgkmcnt(0)
	s_waitcnt lgkmcnt(0)
	v_readfirstlane_b32 s49, v4
	v_readfirstlane_b32 s50, v5
	ds_read2_b32 v[6:7], v9 offset1:1
	ds_read2_b32 v[12:13], v12 offset1:1
	ds_read2_b32 v[14:15], v14 offset1:1
	v_cmp_gt_u32_e64 s[18:19], 32, v1
	s_waitcnt lgkmcnt(0)
	s_waitcnt lgkmcnt(0)
	v_readfirstlane_b32 s51, v6
	v_readfirstlane_b32 s52, v7
	s_waitcnt lgkmcnt(0)
	v_readfirstlane_b32 s53, v12
	v_readfirstlane_b32 s54, v13
	s_waitcnt lgkmcnt(0)
	v_readfirstlane_b32 s55, v14
	v_readfirstlane_b32 s56, v15
	v_readfirstlane_b32 s57, v10
	v_readfirstlane_b32 s58, v11
	s_waitcnt lgkmcnt(0)
	s_waitcnt lgkmcnt(0)
	s_barrier
	v_mov_b32_e32 v4, v26
	s_nop 1
	v_add_u32_dpp v4, v4, v4 row_shr:1 row_mask:0xf bank_mask:0xf bound_ctrl:1
	s_nop 1
	v_add_u32_dpp v4, v4, v4 row_shr:2 row_mask:0xf bank_mask:0xf bound_ctrl:1
	s_nop 1
	v_add_u32_dpp v4, v4, v4 row_shr:4 row_mask:0xf bank_mask:0xf bound_ctrl:1
	s_nop 1
	v_add_u32_dpp v4, v4, v4 row_shr:8 row_mask:0xf bank_mask:0xf bound_ctrl:1
	s_nop 1
	v_add_u32_dpp v4, v4, v4 row_bcast:15 row_mask:0xa bank_mask:0xf
	s_nop 1
	v_add_u32_dpp v4, v4, v4 row_bcast:31 row_mask:0xc bank_mask:0xf
	s_and_saveexec_b64 s[14:15], s[12:13]
	v_lshlrev_b32_e32 v5, 2, v35
	ds_write_b32 v5, v4 offset:32256
	s_or_b64 exec, exec, s[14:15]
	s_waitcnt lgkmcnt(0)
	s_barrier
	ds_read_b96 v[18:20], v2 offset:32256
	ds_read_b32 v30, v2 offset:32276
	ds_read_b64 v[22:23], v2 offset:32312
	ds_read2_b32 v[24:25], v3 offset1:1
	v_mov_b32_e32 v2, 0x7e18
	s_load_dwordx2 s[40:41], s[0:1], 0x10
	v_mov_b32_e32 v3, 0x7e28
	ds_read2_b64 v[14:17], v2 offset1:1
	ds_read2_b64 v[10:13], v3 offset1:1
	v_cmp_gt_u32_e64 s[14:15], 64, v0
	v_cmp_eq_u32_e64 s[16:17], 15, v35
	s_waitcnt lgkmcnt(0)
	s_barrier
	s_and_saveexec_b64 s[20:21], vcc
	s_cbranch_execz .LBB0_10
	s_movk_i32 s22, 0xbf
	s_movk_i32 s3, 0x7f
	v_cmp_lt_u32_e32 vcc, s22, v0
	v_cndmask_b32_e64 v7, v18, 0, s[14:15]
	v_sub_u32_e32 v4, v4, v26
	v_cndmask_b32_e32 v5, 0, v20, vcc
	v_cmp_lt_u32_e32 vcc, s3, v0
	v_lshlrev_b32_e32 v2, 2, v0
	v_cndmask_b32_e64 v3, 0, v22, s[16:17]
	v_cndmask_b32_e32 v6, 0, v19, vcc
	v_add3_u32 v4, v4, v7, v6
	v_add3_u32 v3, v4, v5, v3
	ds_write2st64_b32 v2, v8, v26 offset0:112 offset1:116
	ds_write_b32 v2, v3 offset:30720

.LBB0_36:
	s_and_b64 vcc, exec, s[0:1]
	s_cbranch_vccz .LBB0_175
	v_lshrrev_b32_e32 v8, 2, v0
	v_and_b32_e32 v38, 0xf0, v8
	v_and_or_b32 v2, v0, 15, v38
	v_lshlrev_b32_e32 v4, 2, v2
	ds_read2st64_b32 v[2:3], v4 offset0:112 offset1:116
	ds_read_b32 v39, v4 offset:30720
	v_mov_b32_e32 v6, 0
	v_mov_b32_e32 v7, 0
	v_lshlrev_b32_e32 v4, 2, v1
	s_waitcnt lgkmcnt(1)
	v_mul_u32_u24_e32 v5, 0x186c, v38
	v_lshl_add_u32 v50, v5, 2, v4
	v_readlane_b32 s22, v2, 0
	v_readlane_b32 s0, v3, 0
	s_lshl_b32 s22, s22, 2
	s_nop 0
	v_cmp_gt_i32_e32 vcc, s0, v1
	v_add_u32_e32 v51, s22, v50
	s_and_saveexec_b64 s[0:1], vcc
	global_load_dword v7, v51, s[20:21]
	s_mov_b64 exec, s[0:1]
	v_readlane_b32 s22, v2, 1
	v_readlane_b32 s0, v3, 1
	s_lshl_b32 s22, s22, 2
	s_add_u32 s22, s22, 0x61b0
	v_cmp_gt_i32_e32 vcc, s0, v1
	v_add_u32_e32 v51, s22, v50
	s_and_saveexec_b64 s[0:1], vcc
	global_load_dword v6, v51, s[20:21]
	s_mov_b64 exec, s[0:1]
	v_readlane_b32 s22, v2, 2
	v_readlane_b32 s0, v3, 2
	s_lshl_b32 s22, s22, 2
	s_add_u32 s22, s22, 0xc360
	v_cmp_gt_i32_e32 vcc, s0, v1
	v_add_u32_e32 v51, s22, v50
	s_and_saveexec_b64 s[0:1], vcc
	global_load_dword v26, v51, s[20:21]
	s_mov_b64 exec, s[0:1]
	v_readlane_b32 s22, v2, 3
	v_readlane_b32 s0, v3, 3
	s_lshl_b32 s22, s22, 2
	s_add_u32 s22, s22, 0x12510
	v_cmp_gt_i32_e32 vcc, s0, v1
	v_add_u32_e32 v51, s22, v50
	s_and_saveexec_b64 s[0:1], vcc
	global_load_dword v9, v51, s[20:21]
	s_mov_b64 exec, s[0:1]
	v_readlane_b32 s22, v2, 4
	v_readlane_b32 s0, v3, 4
	s_lshl_b32 s22, s22, 2
	s_add_u32 s22, s22, 0x186c0
	v_cmp_gt_i32_e32 vcc, s0, v1
	v_add_u32_e32 v51, s22, v50
	s_and_saveexec_b64 s[0:1], vcc
	global_load_dword v28, v51, s[20:21]
	s_mov_b64 exec, s[0:1]
	v_readlane_b32 s22, v2, 5
	v_readlane_b32 s0, v3, 5
	s_lshl_b32 s22, s22, 2
	s_add_u32 s22, s22, 0x1e870
	v_cmp_gt_i32_e32 vcc, s0, v1
	v_add_u32_e32 v51, s22, v50
	s_and_saveexec_b64 s[0:1], vcc
	global_load_dword v27, v51, s[20:21]
	s_mov_b64 exec, s[0:1]
	v_readlane_b32 s22, v2, 6
	v_readlane_b32 s0, v3, 6
	s_lshl_b32 s22, s22, 2
	s_add_u32 s22, s22, 0x24a20
	v_cmp_gt_i32_e32 vcc, s0, v1
	v_add_u32_e32 v51, s22, v50
	s_and_saveexec_b64 s[0:1], vcc
	global_load_dword v40, v51, s[20:21]
	s_mov_b64 exec, s[0:1]
	v_readlane_b32 s22, v2, 7
	v_readlane_b32 s0, v3, 7
	s_lshl_b32 s22, s22, 2
	s_add_u32 s22, s22, 0x2abd0
	v_cmp_gt_i32_e32 vcc, s0, v1
	v_add_u32_e32 v51, s22, v50
	s_and_saveexec_b64 s[0:1], vcc
	global_load_dword v29, v51, s[20:21]
	s_mov_b64 exec, s[0:1]
	v_readlane_b32 s22, v2, 8
	v_readlane_b32 s0, v3, 8
	s_lshl_b32 s22, s22, 2
	s_add_u32 s22, s22, 0x30d80
	v_cmp_gt_i32_e32 vcc, s0, v1
	v_add_u32_e32 v51, s22, v50
	s_and_saveexec_b64 s[0:1], vcc
	global_load_dword v42, v51, s[20:21]
	s_mov_b64 exec, s[0:1]
	v_readlane_b32 s22, v2, 9
	v_readlane_b32 s0, v3, 9
	s_lshl_b32 s22, s22, 2
	s_add_u32 s22, s22, 0x36f30
	v_cmp_gt_i32_e32 vcc, s0, v1
	v_add_u32_e32 v51, s22, v50
	s_and_saveexec_b64 s[0:1], vcc
	global_load_dword v41, v51, s[20:21]
	s_mov_b64 exec, s[0:1]
	v_readlane_b32 s22, v2, 10
	v_readlane_b32 s0, v3, 10
	s_lshl_b32 s22, s22, 2
	s_add_u32 s22, s22, 0x3d0e0
	v_cmp_gt_i32_e32 vcc, s0, v1
	v_add_u32_e32 v51, s22, v50
	s_and_saveexec_b64 s[0:1], vcc
	global_load_dword v44, v51, s[20:21]
	s_mov_b64 exec, s[0:1]
	v_readlane_b32 s22, v2, 11
	v_readlane_b32 s0, v3, 11
	s_lshl_b32 s22, s22, 2
	s_add_u32 s22, s22, 0x43290
	v_cmp_gt_i32_e32 vcc, s0, v1
	v_add_u32_e32 v51, s22, v50
	s_and_saveexec_b64 s[0:1], vcc
	global_load_dword v43, v51, s[20:21]
	s_mov_b64 exec, s[0:1]
	v_readlane_b32 s22, v2, 12
	v_readlane_b32 s0, v3, 12
	s_lshl_b32 s22, s22, 2
	s_add_u32 s22, s22, 0x49440
	v_cmp_gt_i32_e32 vcc, s0, v1
	v_add_u32_e32 v51, s22, v50
	s_and_saveexec_b64 s[0:1], vcc
	global_load_dword v46, v51, s[20:21]
	s_mov_b64 exec, s[0:1]
	v_readlane_b32 s22, v2, 13
	v_readlane_b32 s0, v3, 13
	s_lshl_b32 s22, s22, 2
	s_add_u32 s22, s22, 0x4f5f0
	v_cmp_gt_i32_e32 vcc, s0, v1
	v_add_u32_e32 v51, s22, v50
	s_and_saveexec_b64 s[0:1], vcc
	global_load_dword v45, v51, s[20:21]
	s_mov_b64 exec, s[0:1]
	v_readlane_b32 s22, v2, 14
	v_readlane_b32 s0, v3, 14
	s_lshl_b32 s22, s22, 2
	s_add_u32 s22, s22, 0x557a0
	v_cmp_gt_i32_e32 vcc, s0, v1
	v_add_u32_e32 v51, s22, v50
	s_and_saveexec_b64 s[0:1], vcc
	global_load_dword v48, v51, s[20:21]
	s_mov_b64 exec, s[0:1]
	v_readlane_b32 s22, v2, 15
	v_readlane_b32 s0, v3, 15
	s_lshl_b32 s22, s22, 2
	s_add_u32 s22, s22, 0x5b950
	v_cmp_gt_i32_e32 vcc, s0, v1
	v_add_u32_e32 v51, s22, v50
	s_and_saveexec_b64 s[0:1], vcc
	global_load_dword v47, v51, s[20:21]
	s_mov_b64 exec, s[0:1]

.LBB0_101:
	s_or_b64 exec, exec, s[0:1]
	s_waitcnt vmcnt(0)
	v_cmp_lt_i32_e32 vcc, 64, v3
	s_nop 0
	s_cbranch_vccz .LBB0_116
	v_mov_b32_e32 v6, 0x100
	v_lshl_or_b32 v40, v1, 2, v6
	s_mov_b32 s0, 0x61b00
	v_mov_b64_e32 v[6:7], s[20:21]
	v_mad_u64_u32 v[6:7], s[0:1], v35, s0, v[6:7]
	v_or_b32_e32 v4, 64, v1
	v_or_b32_e32 v5, 0x80, v1
	s_mov_b32 s3, 0
	s_movk_i32 s60, 0xbf
	s_movk_i32 s61, 0x186c
	v_mov_b32_e32 v9, 0
	s_mov_b64 s[0:1], 0x100
	s_mov_b64 s[22:23], 0x61b0
	s_branch .LBB0_103

.LBB0_116:
	v_cmp_lt_i32_e32 vcc, v0, v21
	v_mov_b32_e32 v7, -1
	s_waitcnt lgkmcnt(0)
	s_barrier
	v_lshlrev_b32_e32 v54, 2, v0
	v_mov_b32_e32 v28, -1
	v_mov_b32_e32 v38, -1
	v_mov_b32_e32 v40, -1
	v_mov_b32_e32 v42, -1
	v_mov_b32_e32 v44, -1
	v_mov_b32_e32 v46, -1
	v_or_b32_e32 v1, 0x400, v0
	s_and_saveexec_b64 s[0:1], vcc
	ds_read_b32 v7, v54
	s_mov_b64 exec, s[0:1]
	v_cmp_lt_i32_e64 s[42:43], v1, v21
	v_or_b32_e32 v1, 0x800, v0
	s_and_saveexec_b64 s[0:1], s[42:43]
	ds_read_b32 v28, v54 offset:4096
	s_mov_b64 exec, s[0:1]
	v_cmp_lt_i32_e64 s[42:43], v1, v21
	v_or_b32_e32 v1, 0xc00, v0
	s_and_saveexec_b64 s[0:1], s[42:43]
	ds_read_b32 v38, v54 offset:8192
	s_mov_b64 exec, s[0:1]
	v_cmp_lt_i32_e64 s[42:43], v1, v21
	v_or_b32_e32 v1, 0x1000, v0
	s_and_saveexec_b64 s[0:1], s[42:43]
	ds_read_b32 v40, v54 offset:12288
	s_mov_b64 exec, s[0:1]
	v_cmp_lt_i32_e64 s[42:43], v1, v21
	v_or_b32_e32 v1, 0x1400, v0
	s_and_saveexec_b64 s[0:1], s[42:43]
	ds_read_b32 v42, v54 offset:16384
	s_mov_b64 exec, s[0:1]
	v_cmp_lt_i32_e64 s[42:43], v1, v21
	v_or_b32_e32 v1, 0x1800, v0
	s_and_saveexec_b64 s[0:1], s[42:43]
	ds_read_b32 v44, v54 offset:20480
	s_mov_b64 exec, s[0:1]
	v_cmp_lt_i32_e64 s[42:43], v1, v21
	s_nop 0
	s_and_saveexec_b64 s[0:1], s[42:43]
	ds_read_b32 v46, v54 offset:24576
	s_mov_b64 exec, s[0:1]
	v_mov_b32_e32 v2, 0
	v_mov_b32_e32 v1, 0
	v_mov_b32_e32 v4, 0
	v_mov_b32_e32 v3, 0
	v_mov_b32_e32 v6, 0
	v_mov_b32_e32 v5, 0
	v_mov_b32_e32 v8, 0
	v_mov_b32_e32 v54, 1
	s_waitcnt lgkmcnt(0)
	v_cmp_ne_u32_e64 s[20:21], -1, v7
	v_lshrrev_b32_e32 v9, 14, v7
	v_cmp_ne_u32_e64 s[22:23], -1, v28
	v_lshrrev_b32_e32 v29, 14, v28
	v_cmp_ne_u32_e64 s[24:25], -1, v38
	v_lshrrev_b32_e32 v39, 14, v38
	v_cmp_ne_u32_e64 s[26:27], -1, v40
	v_lshrrev_b32_e32 v41, 14, v40
	v_cmp_ne_u32_e64 s[0:1], -1, v42
	v_lshrrev_b32_e32 v43, 14, v42
	v_cmp_ne_u32_e64 s[30:31], -1, v44
	v_lshrrev_b32_e32 v45, 14, v44
	v_cmp_ne_u32_e64 s[34:35], -1, v46
	v_lshrrev_b32_e32 v47, 14, v46
	s_and_saveexec_b64 s[42:43], s[20:21]
	v_and_b32_e32 v2, 0x1fc, v9
	ds_add_rtn_u32 v2, v2, v54 offset:31744
	s_mov_b64 exec, s[42:43]
	s_and_saveexec_b64 s[42:43], s[22:23]
	v_and_b32_e32 v1, 0x1fc, v29
	ds_add_rtn_u32 v1, v1, v54 offset:31744
	s_mov_b64 exec, s[42:43]
	s_and_saveexec_b64 s[42:43], s[24:25]
	v_and_b32_e32 v4, 0x1fc, v39
	ds_add_rtn_u32 v4, v4, v54 offset:31744
	s_mov_b64 exec, s[42:43]
	s_and_saveexec_b64 s[42:43], s[26:27]
	v_and_b32_e32 v3, 0x1fc, v41
	ds_add_rtn_u32 v3, v3, v54 offset:31744
	s_mov_b64 exec, s[42:43]
	s_and_saveexec_b64 s[42:43], s[0:1]
	v_and_b32_e32 v6, 0x1fc, v43
	ds_add_rtn_u32 v6, v6, v54 offset:31744
	s_mov_b64 exec, s[42:43]
	s_and_saveexec_b64 s[42:43], s[30:31]
	v_and_b32_e32 v5, 0x1fc, v45
	ds_add_rtn_u32 v5, v5, v54 offset:31744
	s_mov_b64 exec, s[42:43]
	s_and_saveexec_b64 s[42:43], s[34:35]
	v_and_b32_e32 v8, 0x1fc, v47
	ds_add_rtn_u32 v8, v8, v54 offset:31744
	s_mov_b64 exec, s[42:43]
	v_mov_b32_e32 v48, 0
	s_waitcnt lgkmcnt(0)
	s_barrier
	s_and_saveexec_b64 s[42:43], s[28:29]
	v_lshlrev_b32_e32 v26, 2, v0
	ds_read_b32 v48, v26 offset:31744
	s_or_b64 exec, exec, s[42:43]
	s_waitcnt lgkmcnt(0)
	v_mov_b32_e32 v31, v48
	s_nop 1
	v_add_u32_dpp v31, v31, v31 row_shr:1 row_mask:0xf bank_mask:0xf bound_ctrl:1
	s_nop 1
	v_add_u32_dpp v31, v31, v31 row_shr:2 row_mask:0xf bank_mask:0xf bound_ctrl:1
	s_nop 1
	v_add_u32_dpp v31, v31, v31 row_shr:4 row_mask:0xf bank_mask:0xf bound_ctrl:1
	s_nop 1
	v_add_u32_dpp v31, v31, v31 row_shr:8 row_mask:0xf bank_mask:0xf bound_ctrl:1
	s_nop 1
	v_add_u32_dpp v31, v31, v31 row_bcast:15 row_mask:0xa bank_mask:0xf
	s_nop 1
	v_add_u32_dpp v31, v31, v31 row_bcast:31 row_mask:0xc bank_mask:0xf
	s_and_saveexec_b64 s[4:5], s[12:13]
	v_lshlrev_b32_e32 v26, 2, v35
	ds_write_b32 v26, v31 offset:32256
	s_or_b64 exec, exec, s[4:5]
	s_movk_i32 s3, 0x7c00
	v_add_u32_e64 v26, s3, 0
	s_waitcnt lgkmcnt(0)
	s_barrier
	ds_read2_b32 v[26:27], v26 offset0:128 offset1:142
	s_waitcnt lgkmcnt(0)
	s_barrier
	s_and_saveexec_b64 s[4:5], s[28:29]
	s_cbranch_execz .LBB0_150
	v_lshl_or_b32 v32, s2, 7, v0
	v_sub_u32_e32 v31, v31, v48
	v_cndmask_b32_e64 v27, 0, v27, s[16:17]
	v_cndmask_b32_e64 v26, v26, 0, s[14:15]
	v_ashrrev_i32_e32 v33, 31, v32
	v_add3_u32 v26, v26, v31, v27
	v_lshlrev_b32_e32 v34, 2, v0
	v_lshl_add_u64 v[32:33], v[32:33], 2, s[40:41]
	v_add_u32_e32 v27, s59, v26
	global_store_dword v[32:33], v27, off
	ds_write_b32 v34, v26 offset:31744

.LBB0_152:
	s_or_b64 exec, exec, s[2:3]
	s_waitcnt lgkmcnt(0)
	s_barrier
	v_and_b32_e32 v9, 0x1fc, v9
	v_and_b32_e32 v29, 0x1fc, v29
	v_and_b32_e32 v39, 0x1fc, v39
	v_and_b32_e32 v41, 0x1fc, v41
	v_and_b32_e32 v43, 0x1fc, v43
	v_and_b32_e32 v45, 0x1fc, v45
	v_and_b32_e32 v47, 0x1fc, v47
	ds_read_b32 v9, v9 offset:31744
	ds_read_b32 v29, v29 offset:31744
	ds_read_b32 v39, v39 offset:31744
	ds_read_b32 v41, v41 offset:31744
	ds_read_b32 v43, v43 offset:31744
	ds_read_b32 v45, v45 offset:31744
	ds_read_b32 v47, v47 offset:31744
	v_lshlrev_b32_e32 v2, 2, v2
	v_and_b32_e32 v7, 0xffff, v7
	v_lshlrev_b32_e32 v1, 2, v1
	v_and_b32_e32 v28, 0xffff, v28
	v_lshlrev_b32_e32 v4, 2, v4
	v_and_b32_e32 v38, 0xffff, v38
	v_lshlrev_b32_e32 v3, 2, v3
	v_and_b32_e32 v40, 0xffff, v40
	v_lshlrev_b32_e32 v6, 2, v6
	v_and_b32_e32 v42, 0xffff, v42
	v_lshlrev_b32_e32 v5, 2, v5
	v_and_b32_e32 v44, 0xffff, v44
	v_lshlrev_b32_e32 v8, 2, v8
	v_and_b32_e32 v46, 0xffff, v46
	s_waitcnt lgkmcnt(0)
	v_lshl_add_u32 v2, v9, 2, v2
	v_lshl_add_u32 v1, v29, 2, v1
	v_lshl_add_u32 v4, v39, 2, v4
	v_lshl_add_u32 v3, v41, 2, v3
	v_lshl_add_u32 v6, v43, 2, v6
	v_lshl_add_u32 v5, v45, 2, v5
	v_lshl_add_u32 v8, v47, 2, v8
	s_and_saveexec_b64 s[2:3], s[20:21]
	ds_write_b32 v2, v7
	s_mov_b64 exec, s[2:3]
	s_and_saveexec_b64 s[2:3], s[22:23]
	ds_write_b32 v1, v28
	s_mov_b64 exec, s[2:3]
	s_and_saveexec_b64 s[2:3], s[24:25]
	ds_write_b32 v4, v38
	s_mov_b64 exec, s[2:3]
	s_and_saveexec_b64 s[2:3], s[26:27]
	ds_write_b32 v3, v40
	s_mov_b64 exec, s[2:3]
	s_and_saveexec_b64 s[2:3], s[0:1]
	ds_write_b32 v6, v42
	s_mov_b64 exec, s[2:3]
	s_and_saveexec_b64 s[2:3], s[30:31]
	ds_write_b32 v5, v44
	s_mov_b64 exec, s[2:3]
	s_and_saveexec_b64 s[2:3], s[34:35]
	ds_write_b32 v8, v46
	s_mov_b64 exec, s[2:3]

	.amdhsa_kernel _Z6k_finePKjPKtPiPt
		.amdhsa_group_segment_fixed_size 32320
		.amdhsa_private_segment_fixed_size 0
		.amdhsa_kernarg_size 32
		.amdhsa_user_sgpr_count 2
		.amdhsa_user_sgpr_dispatch_ptr 0
		.amdhsa_user_sgpr_queue_ptr 0
		.amdhsa_user_sgpr_kernarg_segment_ptr 1
		.amdhsa_user_sgpr_dispatch_id 0
		.amdhsa_user_sgpr_kernarg_preload_length 0
		.amdhsa_user_sgpr_kernarg_preload_offset 0
		.amdhsa_user_sgpr_private_segment_size 0
		.amdhsa_uses_dynamic_stack 0
		.amdhsa_enable_private_segment 0
		.amdhsa_system_sgpr_workgroup_id_x 1
		.amdhsa_system_sgpr_workgroup_id_y 0
		.amdhsa_system_sgpr_workgroup_id_z 0
		.amdhsa_system_sgpr_workgroup_info 0
		.amdhsa_system_vgpr_workitem_id 0
		.amdhsa_next_free_vgpr 55
		.amdhsa_next_free_sgpr 65
		.amdhsa_accum_offset 56
		.amdhsa_reserve_vcc 1
		.amdhsa_float_round_mode_32 0
		.amdhsa_float_round_mode_16_64 0
		.amdhsa_float_denorm_mode_32 3
		.amdhsa_float_denorm_mode_16_64 3
		.amdhsa_dx10_clamp 1
		.amdhsa_ieee_mode 1
		.amdhsa_fp16_overflow 0
		.amdhsa_tg_split 0
		.amdhsa_exception_fp_ieee_invalid_op 0
		.amdhsa_exception_fp_denorm_src 0
		.amdhsa_exception_fp_ieee_div_zero 0
		.amdhsa_exception_fp_ieee_overflow 0
		.amdhsa_exception_fp_ieee_underflow 0
		.amdhsa_exception_fp_ieee_inexact 0
		.amdhsa_exception_int_div_zero 0
	.end_amdhsa_kernel

.Lagg2n_w4_a:
	s_waitcnt vmcnt(4)
	ds_read_b128 v[42:45], v75
	v_mov_b32_dpp v16, v0 row_newbcast:5 row_mask:0xf bank_mask:0x3
	v_mov_b32_dpp v16, v0 row_newbcast:13 row_mask:0xf bank_mask:0xc
	v_mov_b32_dpp v17, v4 row_newbcast:5 row_mask:0xf bank_mask:0x3
	v_mov_b32_dpp v17, v4 row_newbcast:13 row_mask:0xf bank_mask:0xc
	v_mov_b32_dpp v18, v8 row_newbcast:5 row_mask:0xf bank_mask:0x3
	v_mov_b32_dpp v18, v8 row_newbcast:13 row_mask:0xf bank_mask:0xc
	v_mov_b32_dpp v19, v12 row_newbcast:5 row_mask:0xf bank_mask:0x3
	v_mov_b32_dpp v19, v12 row_newbcast:13 row_mask:0xf bank_mask:0xc
	s_nop 0
	v_fma_mix_f32 v16, v16, 1.0, v71 op_sel_hi:[1,0,0]
	v_fma_mix_f32 v17, v17, 1.0, v71 op_sel_hi:[1,0,0]
	v_fma_mix_f32 v18, v18, 1.0, v71 op_sel_hi:[1,0,0]
	v_fma_mix_f32 v19, v19, 1.0, v71 op_sel_hi:[1,0,0]
	v_mul_f32_e32 v46, 0x3e4ccccd, v16
	v_mul_f32_e32 v47, 0x3e4ccccd, v17
	v_mul_f32_e32 v48, 0x3e4ccccd, v18
	v_mul_f32_e32 v49, 0x3e4ccccd, v19
	v_max_f32_e32 v16, v16, v46
	v_max_f32_e32 v17, v17, v47
	v_max_f32_e32 v18, v18, v48
	v_max_f32_e32 v19, v19, v49
	v_cmp_lt_i32_e64 s[28:29], 0, v74
	v_cmp_lt_i32_e64 s[30:31], 1, v74
	v_cmp_lt_i32_e64 s[32:33], 2, v74
	v_cmp_lt_i32_e64 s[34:35], 3, v74
	v_cndmask_b32_e64 v16, v51, v16, s[28:29]
	v_cndmask_b32_e64 v17, v51, v17, s[30:31]
	v_cndmask_b32_e64 v18, v51, v18, s[32:33]
	v_cndmask_b32_e64 v19, v51, v19, s[34:35]
	v_max3_f32 v46, v16, v17, v18
	v_max_f32_e32 v46, v46, v19
	v_add_u32_e32 v74, -8, v74
	s_nop 0
	v_mov_b32_dpp v47, v46 row_ror:8 row_mask:0xf bank_mask:0xf
	v_max_f32_e32 v46, v46, v47
	v_max_f32_e32 v47, v33, v46
	v_cmp_neq_f32_e32 vcc, 0xff800000, v47
	s_nop 1
	v_cndmask_b32_e32 v46, 0, v47, vcc
	v_sub_f32_e32 v48, v33, v46
	v_sub_f32_e32 v16, v16, v46
	v_sub_f32_e32 v17, v17, v46
	v_sub_f32_e32 v18, v18, v46
	v_sub_f32_e32 v19, v19, v46
	v_exp_f32_e32 v48, v48
	v_exp_f32_e32 v16, v16
	v_exp_f32_e32 v17, v17
	v_exp_f32_e32 v18, v18
	v_exp_f32_e32 v19, v19
	v_mov_b32_e32 v33, v46
	v_mul_f32_e32 v24, v24, v48
	v_mul_f32_e32 v25, v25, v48
	v_mul_f32_e32 v26, v26, v48
	v_mul_f32_e32 v27, v27, v48
	v_mul_f32_e32 v28, v28, v48
	v_mul_f32_e32 v29, v29, v48
	v_mul_f32_e32 v30, v30, v48
	v_mul_f32_e32 v31, v31, v48
	v_mul_f32_e32 v32, v32, v48
	v_fma_mix_f32 v24, v0, v16, v24 op_sel_hi:[1,0,0]
	v_fma_mix_f32 v25, v0, v16, v25 op_sel:[1,0,0] op_sel_hi:[1,0,0]
	v_fma_mix_f32 v26, v1, v16, v26 op_sel_hi:[1,0,0]
	v_fma_mix_f32 v27, v1, v16, v27 op_sel:[1,0,0] op_sel_hi:[1,0,0]
	v_fma_mix_f32 v28, v2, v16, v28 op_sel_hi:[1,0,0]
	v_fma_mix_f32 v29, v2, v16, v29 op_sel:[1,0,0] op_sel_hi:[1,0,0]
	v_fma_mix_f32 v30, v3, v16, v30 op_sel_hi:[1,0,0]
	v_fma_mix_f32 v31, v3, v16, v31 op_sel:[1,0,0] op_sel_hi:[1,0,0]
	v_fma_mix_f32 v24, v4, v17, v24 op_sel_hi:[1,0,0]
	v_fma_mix_f32 v25, v4, v17, v25 op_sel:[1,0,0] op_sel_hi:[1,0,0]
	v_fma_mix_f32 v26, v5, v17, v26 op_sel_hi:[1,0,0]
	v_fma_mix_f32 v27, v5, v17, v27 op_sel:[1,0,0] op_sel_hi:[1,0,0]
	v_fma_mix_f32 v28, v6, v17, v28 op_sel_hi:[1,0,0]
	v_fma_mix_f32 v29, v6, v17, v29 op_sel:[1,0,0] op_sel_hi:[1,0,0]
	v_fma_mix_f32 v30, v7, v17, v30 op_sel_hi:[1,0,0]
	v_fma_mix_f32 v31, v7, v17, v31 op_sel:[1,0,0] op_sel_hi:[1,0,0]
	v_fma_mix_f32 v24, v8, v18, v24 op_sel_hi:[1,0,0]
	v_fma_mix_f32 v25, v8, v18, v25 op_sel:[1,0,0] op_sel_hi:[1,0,0]
	v_fma_mix_f32 v26, v9, v18, v26 op_sel_hi:[1,0,0]
	v_fma_mix_f32 v27, v9, v18, v27 op_sel:[1,0,0] op_sel_hi:[1,0,0]
	v_fma_mix_f32 v28, v10, v18, v28 op_sel_hi:[1,0,0]
	v_fma_mix_f32 v29, v10, v18, v29 op_sel:[1,0,0] op_sel_hi:[1,0,0]
	v_fma_mix_f32 v30, v11, v18, v30 op_sel_hi:[1,0,0]
	v_fma_mix_f32 v31, v11, v18, v31 op_sel:[1,0,0] op_sel_hi:[1,0,0]
	v_fma_mix_f32 v24, v12, v19, v24 op_sel_hi:[1,0,0]
	v_fma_mix_f32 v25, v12, v19, v25 op_sel:[1,0,0] op_sel_hi:[1,0,0]
	v_fma_mix_f32 v26, v13, v19, v26 op_sel_hi:[1,0,0]
	v_fma_mix_f32 v27, v13, v19, v27 op_sel:[1,0,0] op_sel_hi:[1,0,0]
	v_fma_mix_f32 v28, v14, v19, v28 op_sel_hi:[1,0,0]
	v_fma_mix_f32 v29, v14, v19, v29 op_sel:[1,0,0] op_sel_hi:[1,0,0]
	v_fma_mix_f32 v30, v15, v19, v30 op_sel_hi:[1,0,0]
	v_fma_mix_f32 v31, v15, v19, v31 op_sel:[1,0,0] op_sel_hi:[1,0,0]
	v_add_f32_e32 v46, v16, v17
	v_add_f32_e32 v47, v18, v19
	v_add_f32_e32 v46, v46, v47
	v_add_f32_e32 v32, v32, v46
	s_add_i32 s28, s24, 2
	s_cmp_lt_i32 s28, s23
	s_cbranch_scc0 .Lagg2n_ni_a
	s_waitcnt lgkmcnt(0)
	v_add_u32_e32 v42, v42, v56
	v_add_u32_e32 v43, v43, v56
	v_add_u32_e32 v44, v44, v56
	v_add_u32_e32 v45, v45, v56
	global_load_dwordx4 v[0:3], v42, s[8:9]
	global_load_dwordx4 v[4:7], v43, s[8:9]
	global_load_dwordx4 v[8:11], v44, s[8:9]
	global_load_dwordx4 v[12:15], v45, s[8:9]
	v_add_u32_e32 v75, 32, v75
.Lagg2n_ni_a:
	s_waitcnt lgkmcnt(0)
	s_add_i32 s24, s24, 1
	s_cmp_lt_i32 s24, s23
	s_cbranch_scc0 .Lagg2n_pass_done
	s_add_i32 s28, s24, 1
	s_cmp_lt_i32 s28, s23
	s_cbranch_scc1 .Lagg2n_w4_b
	s_waitcnt vmcnt(0)
.Lagg2n_w4_b:
	s_waitcnt vmcnt(4)
	ds_read_b128 v[42:45], v75
	v_mov_b32_dpp v16, v34 row_newbcast:5 row_mask:0xf bank_mask:0x3
	v_mov_b32_dpp v16, v34 row_newbcast:13 row_mask:0xf bank_mask:0xc
	v_mov_b32_dpp v17, v38 row_newbcast:5 row_mask:0xf bank_mask:0x3
	v_mov_b32_dpp v17, v38 row_newbcast:13 row_mask:0xf bank_mask:0xc
	v_mov_b32_dpp v18, v20 row_newbcast:5 row_mask:0xf bank_mask:0x3
	v_mov_b32_dpp v18, v20 row_newbcast:13 row_mask:0xf bank_mask:0xc
	v_mov_b32_dpp v19, v76 row_newbcast:5 row_mask:0xf bank_mask:0x3
	v_mov_b32_dpp v19, v76 row_newbcast:13 row_mask:0xf bank_mask:0xc
	s_nop 0
	v_fma_mix_f32 v16, v16, 1.0, v71 op_sel_hi:[1,0,0]
	v_fma_mix_f32 v17, v17, 1.0, v71 op_sel_hi:[1,0,0]
	v_fma_mix_f32 v18, v18, 1.0, v71 op_sel_hi:[1,0,0]
	v_fma_mix_f32 v19, v19, 1.0, v71 op_sel_hi:[1,0,0]
	v_mul_f32_e32 v46, 0x3e4ccccd, v16
	v_mul_f32_e32 v47, 0x3e4ccccd, v17
	v_mul_f32_e32 v48, 0x3e4ccccd, v18
	v_mul_f32_e32 v49, 0x3e4ccccd, v19
	v_max_f32_e32 v16, v16, v46
	v_max_f32_e32 v17, v17, v47
	v_max_f32_e32 v18, v18, v48
	v_max_f32_e32 v19, v19, v49
	v_cmp_lt_i32_e64 s[28:29], 0, v74
	v_cmp_lt_i32_e64 s[30:31], 1, v74
	v_cmp_lt_i32_e64 s[32:33], 2, v74
	v_cmp_lt_i32_e64 s[34:35], 3, v74
	v_cndmask_b32_e64 v16, v51, v16, s[28:29]
	v_cndmask_b32_e64 v17, v51, v17, s[30:31]
	v_cndmask_b32_e64 v18, v51, v18, s[32:33]
	v_cndmask_b32_e64 v19, v51, v19, s[34:35]
	v_max3_f32 v46, v16, v17, v18
	v_max_f32_e32 v46, v46, v19
	v_add_u32_e32 v74, -8, v74
	s_nop 0
	v_mov_b32_dpp v47, v46 row_ror:8 row_mask:0xf bank_mask:0xf
	v_max_f32_e32 v46, v46, v47
	v_max_f32_e32 v47, v33, v46
	v_cmp_neq_f32_e32 vcc, 0xff800000, v47
	s_nop 1
	v_cndmask_b32_e32 v46, 0, v47, vcc
	v_sub_f32_e32 v48, v33, v46
	v_sub_f32_e32 v16, v16, v46
	v_sub_f32_e32 v17, v17, v46
	v_sub_f32_e32 v18, v18, v46
	v_sub_f32_e32 v19, v19, v46
	v_exp_f32_e32 v48, v48
	v_exp_f32_e32 v16, v16
	v_exp_f32_e32 v17, v17
	v_exp_f32_e32 v18, v18
	v_exp_f32_e32 v19, v19
	v_mov_b32_e32 v33, v46
	v_mul_f32_e32 v24, v24, v48
	v_mul_f32_e32 v25, v25, v48
	v_mul_f32_e32 v26, v26, v48
	v_mul_f32_e32 v27, v27, v48
	v_mul_f32_e32 v28, v28, v48
	v_mul_f32_e32 v29, v29, v48
	v_mul_f32_e32 v30, v30, v48
	v_mul_f32_e32 v31, v31, v48
	v_mul_f32_e32 v32, v32, v48
	v_fma_mix_f32 v24, v34, v16, v24 op_sel_hi:[1,0,0]
	v_fma_mix_f32 v25, v34, v16, v25 op_sel:[1,0,0] op_sel_hi:[1,0,0]
	v_fma_mix_f32 v26, v35, v16, v26 op_sel_hi:[1,0,0]
	v_fma_mix_f32 v27, v35, v16, v27 op_sel:[1,0,0] op_sel_hi:[1,0,0]
	v_fma_mix_f32 v28, v36, v16, v28 op_sel_hi:[1,0,0]
	v_fma_mix_f32 v29, v36, v16, v29 op_sel:[1,0,0] op_sel_hi:[1,0,0]
	v_fma_mix_f32 v30, v37, v16, v30 op_sel_hi:[1,0,0]
	v_fma_mix_f32 v31, v37, v16, v31 op_sel:[1,0,0] op_sel_hi:[1,0,0]
	v_fma_mix_f32 v24, v38, v17, v24 op_sel_hi:[1,0,0]
	v_fma_mix_f32 v25, v38, v17, v25 op_sel:[1,0,0] op_sel_hi:[1,0,0]
	v_fma_mix_f32 v26, v39, v17, v26 op_sel_hi:[1,0,0]
	v_fma_mix_f32 v27, v39, v17, v27 op_sel:[1,0,0] op_sel_hi:[1,0,0]
	v_fma_mix_f32 v28, v40, v17, v28 op_sel_hi:[1,0,0]
	v_fma_mix_f32 v29, v40, v17, v29 op_sel:[1,0,0] op_sel_hi:[1,0,0]
	v_fma_mix_f32 v30, v41, v17, v30 op_sel_hi:[1,0,0]
	v_fma_mix_f32 v31, v41, v17, v31 op_sel:[1,0,0] op_sel_hi:[1,0,0]
	v_fma_mix_f32 v24, v20, v18, v24 op_sel_hi:[1,0,0]
	v_fma_mix_f32 v25, v20, v18, v25 op_sel:[1,0,0] op_sel_hi:[1,0,0]
	v_fma_mix_f32 v26, v21, v18, v26 op_sel_hi:[1,0,0]
	v_fma_mix_f32 v27, v21, v18, v27 op_sel:[1,0,0] op_sel_hi:[1,0,0]
	v_fma_mix_f32 v28, v22, v18, v28 op_sel_hi:[1,0,0]
	v_fma_mix_f32 v29, v22, v18, v29 op_sel:[1,0,0] op_sel_hi:[1,0,0]
	v_fma_mix_f32 v30, v23, v18, v30 op_sel_hi:[1,0,0]
	v_fma_mix_f32 v31, v23, v18, v31 op_sel:[1,0,0] op_sel_hi:[1,0,0]
	v_fma_mix_f32 v24, v76, v19, v24 op_sel_hi:[1,0,0]
	v_fma_mix_f32 v25, v76, v19, v25 op_sel:[1,0,0] op_sel_hi:[1,0,0]
	v_fma_mix_f32 v26, v77, v19, v26 op_sel_hi:[1,0,0]
	v_fma_mix_f32 v27, v77, v19, v27 op_sel:[1,0,0] op_sel_hi:[1,0,0]
	v_fma_mix_f32 v28, v78, v19, v28 op_sel_hi:[1,0,0]
	v_fma_mix_f32 v29, v78, v19, v29 op_sel:[1,0,0] op_sel_hi:[1,0,0]
	v_fma_mix_f32 v30, v79, v19, v30 op_sel_hi:[1,0,0]
	v_fma_mix_f32 v31, v79, v19, v31 op_sel:[1,0,0] op_sel_hi:[1,0,0]
	v_add_f32_e32 v46, v16, v17
	v_add_f32_e32 v47, v18, v19
	v_add_f32_e32 v46, v46, v47
	v_add_f32_e32 v32, v32, v46
	s_add_i32 s28, s24, 2
	s_cmp_lt_i32 s28, s23
	s_cbranch_scc0 .Lagg2n_ni_b
	s_waitcnt lgkmcnt(0)
	v_add_u32_e32 v42, v42, v56
	v_add_u32_e32 v43, v43, v56
	v_add_u32_e32 v44, v44, v56
	v_add_u32_e32 v45, v45, v56
	global_load_dwordx4 v[34:37], v42, s[8:9]
	global_load_dwordx4 v[38:41], v43, s[8:9]
	global_load_dwordx4 v[20:23], v44, s[8:9]
	global_load_dwordx4 v[76:79], v45, s[8:9]
	v_add_u32_e32 v75, 32, v75
.Lagg2n_ni_b:
	s_waitcnt lgkmcnt(0)
	s_add_i32 s24, s24, 1
	s_cmp_lt_i32 s24, s23
	s_cbranch_scc1 .Lagg2n_loop

amdhsa.kernels:
  - .agpr_count:     0
    .args:
      - .actual_access:  read_only
        .address_space:  global
        .offset:         0
        .size:           8
        .value_kind:     global_buffer
      - .actual_access:  read_only
        .address_space:  global
        .offset:         8
        .size:           8
        .value_kind:     global_buffer
      - .actual_access:  write_only
        .address_space:  global
        .offset:         16
        .size:           8
        .value_kind:     global_buffer
      - .actual_access:  write_only
        .address_space:  global
        .offset:         24
        .size:           8
        .value_kind:     global_buffer
    .group_segment_fixed_size: 32320
    .kernarg_segment_align: 8
    .kernarg_segment_size: 32
    .language:       OpenCL C
    .language_version:
      - 2
      - 0
    .max_flat_workgroup_size: 1024
    .name:           _Z6k_finePKjPKtPiPt
    .private_segment_fixed_size: 0
    .sgpr_count:     71
    .sgpr_spill_count: 0
    .symbol:         _Z6k_finePKjPKtPiPt.kd
    .uniform_work_group_size: 1
    .uses_dynamic_stack: false
    .vgpr_count:     55
    .vgpr_spill_count: 0
    .wavefront_size: 64
  - .agpr_count:     0
    .args:
      - .actual_access:  read_only
        .address_space:  global
        .offset:         0
        .size:           8
        .value_kind:     global_buffer
      - .actual_access:  read_only
        .address_space:  global
        .offset:         8
        .size:           8
        .value_kind:     global_buffer
      - .actual_access:  write_only
        .address_space:  global
        .offset:         16
        .size:           8
        .value_kind:     global_buffer
      - .actual_access:  write_only
        .address_space:  global
        .offset:         24
        .size:           8
        .value_kind:     global_buffer
      - .actual_access:  read_only
        .address_space:  global
        .offset:         32
        .size:           8
        .value_kind:     global_buffer
      - .actual_access:  read_only
        .address_space:  global
        .offset:         40
        .size:           8
        .value_kind:     global_buffer
      - .actual_access:  write_only
        .address_space:  global
        .offset:         48
        .size:           8
        .value_kind:     global_buffer
      - .actual_access:  write_only
        .address_space:  global
        .offset:         56
        .size:           8
        .value_kind:     global_buffer
      - .actual_access:  read_only
        .address_space:  global
        .offset:         64
        .size:           8
        .value_kind:     global_buffer
      - .actual_access:  read_only
        .address_space:  global
        .offset:         72
        .size:           8
        .value_kind:     global_buffer
      - .actual_access:  read_only
        .address_space:  global
        .offset:         80
        .size:           8
        .value_kind:     global_buffer
      - .actual_access:  write_only
        .address_space:  global
        .offset:         88
        .size:           8
        .value_kind:     global_buffer
      - .actual_access:  write_only
        .address_space:  global
        .offset:         96
        .size:           8
        .value_kind:     global_buffer
      - .actual_access:  write_only
        .address_space:  global
        .offset:         104
        .size:           8
        .value_kind:     global_buffer
    .group_segment_fixed_size: 53248
    .kernarg_segment_align: 8
    .kernarg_segment_size: 112
    .language:       OpenCL C
    .language_version:
      - 2
      - 0
    .max_flat_workgroup_size: 256
    .name:           _Z8k_stageAPKiS0_PjPtPKfS4_PDF16_S5_S4_S4_S4_S5_PfS6_
    .private_segment_fixed_size: 0
    .sgpr_count:     75
    .sgpr_spill_count: 0
    .symbol:         _Z8k_stageAPKiS0_PjPtPKfS4_PDF16_S5_S4_S4_S4_S5_PfS6_.kd
    .uniform_work_group_size: 1
    .uses_dynamic_stack: false
    .vgpr_count:     158
    .vgpr_spill_count: 0
    .wavefront_size: 64
  - .agpr_count:     4
    .args:
      - .actual_access:  read_only
        .address_space:  global
        .offset:         0
        .size:           8
        .value_kind:     global_buffer
      - .actual_access:  read_only
        .address_space:  global
        .offset:         8
        .size:           8
        .value_kind:     global_buffer
      - .actual_access:  read_only
        .address_space:  global
        .offset:         16
        .size:           8
        .value_kind:     global_buffer
      - .actual_access:  read_only
        .address_space:  global
        .offset:         24
        .size:           8
        .value_kind:     global_buffer
      - .actual_access:  write_only
        .address_space:  global
        .offset:         32
        .size:           8
        .value_kind:     global_buffer
      - .actual_access:  write_only
        .address_space:  global
        .offset:         40
        .size:           8
        .value_kind:     global_buffer
      - .actual_access:  write_only
        .address_space:  global
        .offset:         48
        .size:           8
        .value_kind:     global_buffer
    .group_segment_fixed_size: 19584
    .kernarg_segment_align: 8
    .kernarg_segment_size: 56
    .language:       OpenCL C
    .language_version:
      - 2
      - 0
    .max_flat_workgroup_size: 256
    .name:           _Z7k_gemm2PKDF16_S0_PKfS2_PDF16_PfS4_
    .private_segment_fixed_size: 0
    .sgpr_count:     30
    .sgpr_spill_count: 0
    .symbol:         _Z7k_gemm2PKDF16_S0_PKfS2_PDF16_PfS4_.kd
    .uniform_work_group_size: 1
    .uses_dynamic_stack: false
    .vgpr_count:     84
    .vgpr_spill_count: 0
    .wavefront_size: 64
  - .agpr_count:     12
    .args:
      - .actual_access:  read_only
        .address_space:  global
        .offset:         0
        .size:           8
        .value_kind:     global_buffer
      - .actual_access:  read_only
        .address_space:  global
        .offset:         8
        .size:           8
        .value_kind:     global_buffer
      - .actual_access:  read_only
        .address_space:  global
        .offset:         16
        .size:           8
        .value_kind:     global_buffer
      - .actual_access:  read_only
        .address_space:  global
        .offset:         24
        .size:           8
        .value_kind:     global_buffer
      - .actual_access:  read_only
        .address_space:  global
        .offset:         32
        .size:           8
        .value_kind:     global_buffer
      - .actual_access:  read_only
        .address_space:  global
        .offset:         40
        .size:           8
        .value_kind:     global_buffer
      - .actual_access:  read_only
        .address_space:  global
        .offset:         48
        .size:           8
        .value_kind:     global_buffer
      - .actual_access:  read_only
        .address_space:  global
        .offset:         56
        .size:           8
        .value_kind:     global_buffer
      - .actual_access:  read_only
        .address_space:  global
        .offset:         64
        .size:           8
        .value_kind:     global_buffer
      - .actual_access:  read_only
        .address_space:  global
        .offset:         72
        .size:           8
        .value_kind:     global_buffer
      - .actual_access:  write_only
        .address_space:  global
        .offset:         80
        .size:           8
        .value_kind:     global_buffer
      - .actual_access:  write_only
        .address_space:  global
        .offset:         88
        .size:           8
        .value_kind:     global_buffer
      - .actual_access:  write_only
        .address_space:  global
        .offset:         96
        .size:           8
        .value_kind:     global_buffer
      - .offset:         104
        .size:           4
        .value_kind:     hidden_block_count_x
      - .offset:         108
        .size:           4
        .value_kind:     hidden_block_count_y
      - .offset:         112
        .size:           4
        .value_kind:     hidden_block_count_z
      - .offset:         116
        .size:           2
        .value_kind:     hidden_group_size_x
      - .offset:         118
        .size:           2
        .value_kind:     hidden_group_size_y
      - .offset:         120
        .size:           2
        .value_kind:     hidden_group_size_z
      - .offset:         122
        .size:           2
        .value_kind:     hidden_remainder_x
      - .offset:         124
        .size:           2
        .value_kind:     hidden_remainder_y
      - .offset:         126
        .size:           2
        .value_kind:     hidden_remainder_z
      - .offset:         144
        .size:           8
        .value_kind:     hidden_global_offset_x
      - .offset:         152
        .size:           8
        .value_kind:     hidden_global_offset_y
      - .offset:         160
        .size:           8
        .value_kind:     hidden_global_offset_z
      - .offset:         168
        .size:           2
        .value_kind:     hidden_grid_dims
    .group_segment_fixed_size: 39168
    .kernarg_segment_align: 8
    .kernarg_segment_size: 360
    .language:       OpenCL C
    .language_version:
      - 2
      - 0
    .max_flat_workgroup_size: 256
    .name:           _Z5k_aggILi4ELi128ELi16ELi16ELb0EEvPKiPKtPKDF16_PKfS7_S7_PvS5_S7_S7_PDF16_PfSA_
    .private_segment_fixed_size: 0
    .sgpr_count:     55
    .sgpr_spill_count: 0
    .symbol:         _Z5k_aggILi4ELi128ELi16ELi16ELb0EEvPKiPKtPKDF16_PKfS7_S7_PvS5_S7_S7_PDF16_PfSA_.kd
    .uniform_work_group_size: 1
    .uses_dynamic_stack: false
    .vgpr_count:     124
    .vgpr_spill_count: 0
    .wavefront_size: 64
  - .agpr_count:     0
    .args:
      - .actual_access:  read_only
        .address_space:  global
        .offset:         0
        .size:           8
        .value_kind:     global_buffer
      - .actual_access:  read_only
        .address_space:  global
        .offset:         8
        .size:           8
        .value_kind:     global_buffer
      - .actual_access:  read_only
        .address_space:  global
        .offset:         16
        .size:           8
        .value_kind:     global_buffer
      - .actual_access:  read_only
        .address_space:  global
        .offset:         24
        .size:           8
        .value_kind:     global_buffer
      - .actual_access:  read_only
        .address_space:  global
        .offset:         32
        .size:           8
        .value_kind:     global_buffer
      - .actual_access:  read_only
        .address_space:  global
        .offset:         40
        .size:           8
        .value_kind:     global_buffer
      - .actual_access:  write_only
        .address_space:  global
        .offset:         48
        .size:           8
        .value_kind:     global_buffer
      - .actual_access:  read_only
        .address_space:  global
        .offset:         56
        .size:           8
        .value_kind:     global_buffer
      - .actual_access:  read_only
        .address_space:  global
        .offset:         64
        .size:           8
        .value_kind:     global_buffer
      - .actual_access:  read_only
        .address_space:  global
        .offset:         72
        .size:           8
        .value_kind:     global_buffer
      - .actual_access:  read_only
        .address_space:  global
        .offset:         80
        .size:           8
        .value_kind:     global_buffer
      - .actual_access:  read_only
        .address_space:  global
        .offset:         88
        .size:           8
        .value_kind:     global_buffer
      - .actual_access:  read_only
        .address_space:  global
        .offset:         96
        .size:           8
        .value_kind:     global_buffer
      - .offset:         104
        .size:           4
        .value_kind:     hidden_block_count_x
      - .offset:         108
        .size:           4
        .value_kind:     hidden_block_count_y
      - .offset:         112
        .size:           4
        .value_kind:     hidden_block_count_z
      - .offset:         116
        .size:           2
        .value_kind:     hidden_group_size_x
      - .offset:         118
        .size:           2
        .value_kind:     hidden_group_size_y
      - .offset:         120
        .size:           2
        .value_kind:     hidden_group_size_z
      - .offset:         122
        .size:           2
        .value_kind:     hidden_remainder_x
      - .offset:         124
        .size:           2
        .value_kind:     hidden_remainder_y
      - .offset:         126
        .size:           2
        .value_kind:     hidden_remainder_z
      - .offset:         144
        .size:           8
        .value_kind:     hidden_global_offset_x
      - .offset:         152
        .size:           8
        .value_kind:     hidden_global_offset_y
      - .offset:         160
        .size:           8
        .value_kind:     hidden_global_offset_z
      - .offset:         168
        .size:           2
        .value_kind:     hidden_grid_dims
    .group_segment_fixed_size: 8704
    .kernarg_segment_align: 8
    .kernarg_segment_size: 360
    .language:       OpenCL C
    .language_version:
      - 2
      - 0
    .max_flat_workgroup_size: 256
    .name:           _Z5k_aggILi1ELi40ELi5ELi5ELb1EEvPKiPKtPKDF16_PKfS7_S7_PvS5_S7_S7_PDF16_PfSA_
    .private_segment_fixed_size: 0
    .sgpr_count:     46
    .sgpr_spill_count: 0
    .symbol:         _Z5k_aggILi1ELi40ELi5ELi5ELb1EEvPKiPKtPKDF16_PKfS7_S7_PvS5_S7_S7_PDF16_PfSA_.kd
    .uniform_work_group_size: 1
    .uses_dynamic_stack: false
    .vgpr_count:     80
    .vgpr_spill_count: 0
    .wavefront_size: 64
